# merge GEMM mid-K hook rewritten by hand: all 32 gate loads issued together with counted vmcnt waits (one memory round trip instead of four), same arithmetic; on top of the conflict-free LDS fragment r
# speedup vs baseline: 1.0119x; 1.0119x over previous
.LBB0_630:
	v_mov_b32_e32 v3, v188
	v_mov_b32_e32 v5, v170
	s_movk_i32 s66, 0x2600
	s_mov_b64 s[68:69], 0x80
	v_lshl_add_u32 v4, v3, 3, s52
	v_add_u32_e32 v3, s13, v5
	v_add_u32_e32 v5, s22, v4
	v_add_u32_e32 v4, s26, v4
	s_nop 15
	v_mov_b32_e32 v6, v3
	v_mad_u32_u24 v7, v6, s66, v4
	v_mad_u32_u24 v6, v6, s66, v5
	global_load_dwordx2 v[8:9], v7, s[2:3]
	global_load_dwordx2 v[10:11], v6, s[2:3]
	global_load_dwordx2 v[12:13], v7, s[2:3] offset:128
	global_load_dwordx2 v[14:15], v6, s[2:3] offset:128
	v_add_u32_e32 v6, 16, v3
	v_mad_u32_u24 v7, v6, s66, v4
	v_mad_u32_u24 v6, v6, s66, v5
	global_load_dwordx2 v[16:17], v7, s[2:3]
	global_load_dwordx2 v[18:19], v6, s[2:3]
	global_load_dwordx2 v[20:21], v7, s[2:3] offset:128
	global_load_dwordx2 v[22:23], v6, s[2:3] offset:128
	v_add_u32_e32 v6, 32, v3
	v_mad_u32_u24 v7, v6, s66, v4
	v_mad_u32_u24 v6, v6, s66, v5
	global_load_dwordx2 v[24:25], v7, s[2:3]
	global_load_dwordx2 v[26:27], v6, s[2:3]
	global_load_dwordx2 v[28:29], v7, s[2:3] offset:128
	global_load_dwordx2 v[30:31], v6, s[2:3] offset:128
	v_add_u32_e32 v6, 48, v3
	v_mad_u32_u24 v7, v6, s66, v4
	v_mad_u32_u24 v6, v6, s66, v5
	global_load_dwordx2 v[32:33], v7, s[2:3]
	global_load_dwordx2 v[34:35], v6, s[2:3]
	global_load_dwordx2 v[164:165], v7, s[2:3] offset:128
	global_load_dwordx2 v[166:167], v6, s[2:3] offset:128
	v_add_u32_e32 v6, 128, v3
	v_mad_u32_u24 v7, v6, s66, v4
	v_mad_u32_u24 v6, v6, s66, v5
	global_load_dwordx2 v[180:181], v7, s[2:3]
	global_load_dwordx2 v[182:183], v6, s[2:3]
	global_load_dwordx2 v[184:185], v7, s[2:3] offset:128
	global_load_dwordx2 v[186:187], v6, s[2:3] offset:128
	v_add_u32_e32 v6, 144, v3
	v_mad_u32_u24 v7, v6, s66, v4
	v_mad_u32_u24 v6, v6, s66, v5
	global_load_dwordx2 v[192:193], v7, s[2:3]
	global_load_dwordx2 v[194:195], v6, s[2:3]
	global_load_dwordx2 v[196:197], v7, s[2:3] offset:128
	global_load_dwordx2 v[198:199], v6, s[2:3] offset:128
	v_add_u32_e32 v6, 160, v3
	v_mad_u32_u24 v7, v6, s66, v4
	v_mad_u32_u24 v6, v6, s66, v5
	global_load_dwordx2 v[200:201], v7, s[2:3]
	global_load_dwordx2 v[202:203], v6, s[2:3]
	global_load_dwordx2 v[204:205], v7, s[2:3] offset:128
	global_load_dwordx2 v[206:207], v6, s[2:3] offset:128
	v_add_u32_e32 v6, 176, v3
	v_mad_u32_u24 v7, v6, s66, v4
	v_mad_u32_u24 v6, v6, s66, v5
	global_load_dwordx2 v[226:227], v7, s[2:3]
	global_load_dwordx2 v[228:229], v6, s[2:3]
	global_load_dwordx2 v[230:231], v7, s[2:3] offset:128
	global_load_dwordx2 v[232:233], v6, s[2:3] offset:128
	s_waitcnt vmcnt(30)
	v_cvt_f32_ubyte0_e32 v234, v10
	v_cvt_f32_ubyte1_e32 v235, v10
	v_cvt_f32_ubyte2_e32 v236, v10
	v_cvt_f32_ubyte3_e32 v237, v10
	v_rcp_iflag_f32_e32 v234, v234
	v_rcp_iflag_f32_e32 v235, v235
	v_rcp_iflag_f32_e32 v236, v236
	v_rcp_iflag_f32_e32 v237, v237
	v_cvt_f32_ubyte0_e32 v238, v8
	v_cvt_f32_ubyte1_e32 v239, v8
	v_cvt_f32_ubyte2_e32 v240, v8
	v_cvt_f32_ubyte3_e32 v241, v8
	v_pk_mul_f32 v[234:235], v[234:235], v[238:239]
	v_pk_mul_f32 v[236:237], v[236:237], v[240:241]
	v_pk_mul_f32 v[160:161], v[160:161], v[234:235]
	v_pk_mul_f32 v[162:163], v[162:163], v[236:237]
	v_cvt_f32_ubyte0_e32 v234, v11
	v_cvt_f32_ubyte1_e32 v235, v11
	v_cvt_f32_ubyte2_e32 v236, v11
	v_cvt_f32_ubyte3_e32 v237, v11
	v_rcp_iflag_f32_e32 v234, v234
	v_rcp_iflag_f32_e32 v235, v235
	v_rcp_iflag_f32_e32 v236, v236
	v_rcp_iflag_f32_e32 v237, v237
	v_cvt_f32_ubyte0_e32 v238, v9
	v_cvt_f32_ubyte1_e32 v239, v9
	v_cvt_f32_ubyte2_e32 v240, v9
	v_cvt_f32_ubyte3_e32 v241, v9
	v_pk_mul_f32 v[234:235], v[234:235], v[238:239]
	v_pk_mul_f32 v[236:237], v[236:237], v[240:241]
	v_pk_mul_f32 v[156:157], v[156:157], v[234:235]
	v_pk_mul_f32 v[158:159], v[158:159], v[236:237]
	s_waitcnt vmcnt(28)
	v_cvt_f32_ubyte0_e32 v234, v14
	v_cvt_f32_ubyte1_e32 v235, v14
	v_cvt_f32_ubyte2_e32 v236, v14
	v_cvt_f32_ubyte3_e32 v237, v14
	v_rcp_iflag_f32_e32 v234, v234
	v_rcp_iflag_f32_e32 v235, v235
	v_rcp_iflag_f32_e32 v236, v236
	v_rcp_iflag_f32_e32 v237, v237
	v_cvt_f32_ubyte0_e32 v238, v12
	v_cvt_f32_ubyte1_e32 v239, v12
	v_cvt_f32_ubyte2_e32 v240, v12
	v_cvt_f32_ubyte3_e32 v241, v12
	v_pk_mul_f32 v[234:235], v[234:235], v[238:239]
	v_pk_mul_f32 v[236:237], v[236:237], v[240:241]
	v_pk_mul_f32 v[152:153], v[152:153], v[234:235]
	v_pk_mul_f32 v[154:155], v[154:155], v[236:237]
	v_cvt_f32_ubyte0_e32 v234, v15
	v_cvt_f32_ubyte1_e32 v235, v15
	v_cvt_f32_ubyte2_e32 v236, v15
	v_cvt_f32_ubyte3_e32 v237, v15
	v_rcp_iflag_f32_e32 v234, v234
	v_rcp_iflag_f32_e32 v235, v235
	v_rcp_iflag_f32_e32 v236, v236
	v_rcp_iflag_f32_e32 v237, v237
	v_cvt_f32_ubyte0_e32 v238, v13
	v_cvt_f32_ubyte1_e32 v239, v13
	v_cvt_f32_ubyte2_e32 v240, v13
	v_cvt_f32_ubyte3_e32 v241, v13
	v_pk_mul_f32 v[234:235], v[234:235], v[238:239]
	v_pk_mul_f32 v[236:237], v[236:237], v[240:241]
	v_pk_mul_f32 v[148:149], v[148:149], v[234:235]
	v_pk_mul_f32 v[150:151], v[150:151], v[236:237]
	s_waitcnt vmcnt(26)
	v_cvt_f32_ubyte0_e32 v234, v18
	v_cvt_f32_ubyte1_e32 v235, v18
	v_cvt_f32_ubyte2_e32 v236, v18
	v_cvt_f32_ubyte3_e32 v237, v18
	v_rcp_iflag_f32_e32 v234, v234
	v_rcp_iflag_f32_e32 v235, v235
	v_rcp_iflag_f32_e32 v236, v236
	v_rcp_iflag_f32_e32 v237, v237
	v_cvt_f32_ubyte0_e32 v238, v16
	v_cvt_f32_ubyte1_e32 v239, v16
	v_cvt_f32_ubyte2_e32 v240, v16
	v_cvt_f32_ubyte3_e32 v241, v16
	v_pk_mul_f32 v[234:235], v[234:235], v[238:239]
	v_pk_mul_f32 v[236:237], v[236:237], v[240:241]
	v_pk_mul_f32 v[144:145], v[144:145], v[234:235]
	v_pk_mul_f32 v[146:147], v[146:147], v[236:237]
	v_cvt_f32_ubyte0_e32 v234, v19
	v_cvt_f32_ubyte1_e32 v235, v19
	v_cvt_f32_ubyte2_e32 v236, v19
	v_cvt_f32_ubyte3_e32 v237, v19
	v_rcp_iflag_f32_e32 v234, v234
	v_rcp_iflag_f32_e32 v235, v235
	v_rcp_iflag_f32_e32 v236, v236
	v_rcp_iflag_f32_e32 v237, v237
	v_cvt_f32_ubyte0_e32 v238, v17
	v_cvt_f32_ubyte1_e32 v239, v17
	v_cvt_f32_ubyte2_e32 v240, v17
	v_cvt_f32_ubyte3_e32 v241, v17
	v_pk_mul_f32 v[234:235], v[234:235], v[238:239]
	v_pk_mul_f32 v[236:237], v[236:237], v[240:241]
	v_pk_mul_f32 v[140:141], v[140:141], v[234:235]
	v_pk_mul_f32 v[142:143], v[142:143], v[236:237]
	s_waitcnt vmcnt(24)
	v_cvt_f32_ubyte0_e32 v234, v22
	v_cvt_f32_ubyte1_e32 v235, v22
	v_cvt_f32_ubyte2_e32 v236, v22
	v_cvt_f32_ubyte3_e32 v237, v22
	v_rcp_iflag_f32_e32 v234, v234
	v_rcp_iflag_f32_e32 v235, v235
	v_rcp_iflag_f32_e32 v236, v236
	v_rcp_iflag_f32_e32 v237, v237
	v_cvt_f32_ubyte0_e32 v238, v20
	v_cvt_f32_ubyte1_e32 v239, v20
	v_cvt_f32_ubyte2_e32 v240, v20
	v_cvt_f32_ubyte3_e32 v241, v20
	v_pk_mul_f32 v[234:235], v[234:235], v[238:239]
	v_pk_mul_f32 v[236:237], v[236:237], v[240:241]
	v_pk_mul_f32 v[136:137], v[136:137], v[234:235]
	v_pk_mul_f32 v[138:139], v[138:139], v[236:237]
	v_cvt_f32_ubyte0_e32 v234, v23
	v_cvt_f32_ubyte1_e32 v235, v23
	v_cvt_f32_ubyte2_e32 v236, v23
	v_cvt_f32_ubyte3_e32 v237, v23
	v_rcp_iflag_f32_e32 v234, v234
	v_rcp_iflag_f32_e32 v235, v235
	v_rcp_iflag_f32_e32 v236, v236
	v_rcp_iflag_f32_e32 v237, v237
	v_cvt_f32_ubyte0_e32 v238, v21
	v_cvt_f32_ubyte1_e32 v239, v21
	v_cvt_f32_ubyte2_e32 v240, v21
	v_cvt_f32_ubyte3_e32 v241, v21
	v_pk_mul_f32 v[234:235], v[234:235], v[238:239]
	v_pk_mul_f32 v[236:237], v[236:237], v[240:241]
	v_pk_mul_f32 v[132:133], v[132:133], v[234:235]
	v_pk_mul_f32 v[134:135], v[134:135], v[236:237]
	s_waitcnt vmcnt(22)
	v_cvt_f32_ubyte0_e32 v234, v26
	v_cvt_f32_ubyte1_e32 v235, v26
	v_cvt_f32_ubyte2_e32 v236, v26
	v_cvt_f32_ubyte3_e32 v237, v26
	v_rcp_iflag_f32_e32 v234, v234
	v_rcp_iflag_f32_e32 v235, v235
	v_rcp_iflag_f32_e32 v236, v236
	v_rcp_iflag_f32_e32 v237, v237
	v_cvt_f32_ubyte0_e32 v238, v24
	v_cvt_f32_ubyte1_e32 v239, v24
	v_cvt_f32_ubyte2_e32 v240, v24
	v_cvt_f32_ubyte3_e32 v241, v24
	v_pk_mul_f32 v[234:235], v[234:235], v[238:239]
	v_pk_mul_f32 v[236:237], v[236:237], v[240:241]
	v_pk_mul_f32 v[128:129], v[128:129], v[234:235]
	v_pk_mul_f32 v[130:131], v[130:131], v[236:237]
	v_cvt_f32_ubyte0_e32 v234, v27
	v_cvt_f32_ubyte1_e32 v235, v27
	v_cvt_f32_ubyte2_e32 v236, v27
	v_cvt_f32_ubyte3_e32 v237, v27
	v_rcp_iflag_f32_e32 v234, v234
	v_rcp_iflag_f32_e32 v235, v235
	v_rcp_iflag_f32_e32 v236, v236
	v_rcp_iflag_f32_e32 v237, v237
	v_cvt_f32_ubyte0_e32 v238, v25
	v_cvt_f32_ubyte1_e32 v239, v25
	v_cvt_f32_ubyte2_e32 v240, v25
	v_cvt_f32_ubyte3_e32 v241, v25
	v_pk_mul_f32 v[234:235], v[234:235], v[238:239]
	v_pk_mul_f32 v[236:237], v[236:237], v[240:241]
	v_pk_mul_f32 v[124:125], v[124:125], v[234:235]
	v_pk_mul_f32 v[126:127], v[126:127], v[236:237]
	s_waitcnt vmcnt(20)
	v_cvt_f32_ubyte0_e32 v234, v30
	v_cvt_f32_ubyte1_e32 v235, v30
	v_cvt_f32_ubyte2_e32 v236, v30
	v_cvt_f32_ubyte3_e32 v237, v30
	v_rcp_iflag_f32_e32 v234, v234
	v_rcp_iflag_f32_e32 v235, v235
	v_rcp_iflag_f32_e32 v236, v236
	v_rcp_iflag_f32_e32 v237, v237
	v_cvt_f32_ubyte0_e32 v238, v28
	v_cvt_f32_ubyte1_e32 v239, v28
	v_cvt_f32_ubyte2_e32 v240, v28
	v_cvt_f32_ubyte3_e32 v241, v28
	v_pk_mul_f32 v[234:235], v[234:235], v[238:239]
	v_pk_mul_f32 v[236:237], v[236:237], v[240:241]
	v_pk_mul_f32 v[120:121], v[120:121], v[234:235]
	v_pk_mul_f32 v[122:123], v[122:123], v[236:237]
	v_cvt_f32_ubyte0_e32 v234, v31
	v_cvt_f32_ubyte1_e32 v235, v31
	v_cvt_f32_ubyte2_e32 v236, v31
	v_cvt_f32_ubyte3_e32 v237, v31
	v_rcp_iflag_f32_e32 v234, v234
	v_rcp_iflag_f32_e32 v235, v235
	v_rcp_iflag_f32_e32 v236, v236
	v_rcp_iflag_f32_e32 v237, v237
	v_cvt_f32_ubyte0_e32 v238, v29
	v_cvt_f32_ubyte1_e32 v239, v29
	v_cvt_f32_ubyte2_e32 v240, v29
	v_cvt_f32_ubyte3_e32 v241, v29
	v_pk_mul_f32 v[234:235], v[234:235], v[238:239]
	v_pk_mul_f32 v[236:237], v[236:237], v[240:241]
	v_pk_mul_f32 v[116:117], v[116:117], v[234:235]
	v_pk_mul_f32 v[118:119], v[118:119], v[236:237]
	s_waitcnt vmcnt(18)
	v_cvt_f32_ubyte0_e32 v234, v34
	v_cvt_f32_ubyte1_e32 v235, v34
	v_cvt_f32_ubyte2_e32 v236, v34
	v_cvt_f32_ubyte3_e32 v237, v34
	v_rcp_iflag_f32_e32 v234, v234
	v_rcp_iflag_f32_e32 v235, v235
	v_rcp_iflag_f32_e32 v236, v236
	v_rcp_iflag_f32_e32 v237, v237
	v_cvt_f32_ubyte0_e32 v238, v32
	v_cvt_f32_ubyte1_e32 v239, v32
	v_cvt_f32_ubyte2_e32 v240, v32
	v_cvt_f32_ubyte3_e32 v241, v32
	v_pk_mul_f32 v[234:235], v[234:235], v[238:239]
	v_pk_mul_f32 v[236:237], v[236:237], v[240:241]
	v_pk_mul_f32 v[112:113], v[112:113], v[234:235]
	v_pk_mul_f32 v[114:115], v[114:115], v[236:237]
	v_cvt_f32_ubyte0_e32 v234, v35
	v_cvt_f32_ubyte1_e32 v235, v35
	v_cvt_f32_ubyte2_e32 v236, v35
	v_cvt_f32_ubyte3_e32 v237, v35
	v_rcp_iflag_f32_e32 v234, v234
	v_rcp_iflag_f32_e32 v235, v235
	v_rcp_iflag_f32_e32 v236, v236
	v_rcp_iflag_f32_e32 v237, v237
	v_cvt_f32_ubyte0_e32 v238, v33
	v_cvt_f32_ubyte1_e32 v239, v33
	v_cvt_f32_ubyte2_e32 v240, v33
	v_cvt_f32_ubyte3_e32 v241, v33
	v_pk_mul_f32 v[234:235], v[234:235], v[238:239]
	v_pk_mul_f32 v[236:237], v[236:237], v[240:241]
	v_pk_mul_f32 v[108:109], v[108:109], v[234:235]
	v_pk_mul_f32 v[110:111], v[110:111], v[236:237]
	s_waitcnt vmcnt(16)
	v_cvt_f32_ubyte0_e32 v234, v166
	v_cvt_f32_ubyte1_e32 v235, v166
	v_cvt_f32_ubyte2_e32 v236, v166
	v_cvt_f32_ubyte3_e32 v237, v166
	v_rcp_iflag_f32_e32 v234, v234
	v_rcp_iflag_f32_e32 v235, v235
	v_rcp_iflag_f32_e32 v236, v236
	v_rcp_iflag_f32_e32 v237, v237
	v_cvt_f32_ubyte0_e32 v238, v164
	v_cvt_f32_ubyte1_e32 v239, v164
	v_cvt_f32_ubyte2_e32 v240, v164
	v_cvt_f32_ubyte3_e32 v241, v164
	v_pk_mul_f32 v[234:235], v[234:235], v[238:239]
	v_pk_mul_f32 v[236:237], v[236:237], v[240:241]
	v_pk_mul_f32 v[104:105], v[104:105], v[234:235]
	v_pk_mul_f32 v[106:107], v[106:107], v[236:237]
	v_cvt_f32_ubyte0_e32 v234, v167
	v_cvt_f32_ubyte1_e32 v235, v167
	v_cvt_f32_ubyte2_e32 v236, v167
	v_cvt_f32_ubyte3_e32 v237, v167
	v_rcp_iflag_f32_e32 v234, v234
	v_rcp_iflag_f32_e32 v235, v235
	v_rcp_iflag_f32_e32 v236, v236
	v_rcp_iflag_f32_e32 v237, v237
	v_cvt_f32_ubyte0_e32 v238, v165
	v_cvt_f32_ubyte1_e32 v239, v165
	v_cvt_f32_ubyte2_e32 v240, v165
	v_cvt_f32_ubyte3_e32 v241, v165
	v_pk_mul_f32 v[234:235], v[234:235], v[238:239]
	v_pk_mul_f32 v[236:237], v[236:237], v[240:241]
	v_pk_mul_f32 v[100:101], v[100:101], v[234:235]
	v_pk_mul_f32 v[102:103], v[102:103], v[236:237]
	s_waitcnt vmcnt(14)
	v_cvt_f32_ubyte0_e32 v234, v182
	v_cvt_f32_ubyte1_e32 v235, v182
	v_cvt_f32_ubyte2_e32 v236, v182
	v_cvt_f32_ubyte3_e32 v237, v182
	v_rcp_iflag_f32_e32 v234, v234
	v_rcp_iflag_f32_e32 v235, v235
	v_rcp_iflag_f32_e32 v236, v236
	v_rcp_iflag_f32_e32 v237, v237
	v_cvt_f32_ubyte0_e32 v238, v180
	v_cvt_f32_ubyte1_e32 v239, v180
	v_cvt_f32_ubyte2_e32 v240, v180
	v_cvt_f32_ubyte3_e32 v241, v180
	v_pk_mul_f32 v[234:235], v[234:235], v[238:239]
	v_pk_mul_f32 v[236:237], v[236:237], v[240:241]
	v_pk_mul_f32 v[96:97], v[96:97], v[234:235]
	v_pk_mul_f32 v[98:99], v[98:99], v[236:237]
	v_cvt_f32_ubyte0_e32 v234, v183
	v_cvt_f32_ubyte1_e32 v235, v183
	v_cvt_f32_ubyte2_e32 v236, v183
	v_cvt_f32_ubyte3_e32 v237, v183
	v_rcp_iflag_f32_e32 v234, v234
	v_rcp_iflag_f32_e32 v235, v235
	v_rcp_iflag_f32_e32 v236, v236
	v_rcp_iflag_f32_e32 v237, v237
	v_cvt_f32_ubyte0_e32 v238, v181
	v_cvt_f32_ubyte1_e32 v239, v181
	v_cvt_f32_ubyte2_e32 v240, v181
	v_cvt_f32_ubyte3_e32 v241, v181
	v_pk_mul_f32 v[234:235], v[234:235], v[238:239]
	v_pk_mul_f32 v[236:237], v[236:237], v[240:241]
	v_pk_mul_f32 v[92:93], v[92:93], v[234:235]
	v_pk_mul_f32 v[94:95], v[94:95], v[236:237]
	s_waitcnt vmcnt(12)
	v_cvt_f32_ubyte0_e32 v234, v186
	v_cvt_f32_ubyte1_e32 v235, v186
	v_cvt_f32_ubyte2_e32 v236, v186
	v_cvt_f32_ubyte3_e32 v237, v186
	v_rcp_iflag_f32_e32 v234, v234
	v_rcp_iflag_f32_e32 v235, v235
	v_rcp_iflag_f32_e32 v236, v236
	v_rcp_iflag_f32_e32 v237, v237
	v_cvt_f32_ubyte0_e32 v238, v184
	v_cvt_f32_ubyte1_e32 v239, v184
	v_cvt_f32_ubyte2_e32 v240, v184
	v_cvt_f32_ubyte3_e32 v241, v184
	v_pk_mul_f32 v[234:235], v[234:235], v[238:239]
	v_pk_mul_f32 v[236:237], v[236:237], v[240:241]
	v_pk_mul_f32 v[88:89], v[88:89], v[234:235]
	v_pk_mul_f32 v[90:91], v[90:91], v[236:237]
	v_cvt_f32_ubyte0_e32 v234, v187
	v_cvt_f32_ubyte1_e32 v235, v187
	v_cvt_f32_ubyte2_e32 v236, v187
	v_cvt_f32_ubyte3_e32 v237, v187
	v_rcp_iflag_f32_e32 v234, v234
	v_rcp_iflag_f32_e32 v235, v235
	v_rcp_iflag_f32_e32 v236, v236
	v_rcp_iflag_f32_e32 v237, v237
	v_cvt_f32_ubyte0_e32 v238, v185
	v_cvt_f32_ubyte1_e32 v239, v185
	v_cvt_f32_ubyte2_e32 v240, v185
	v_cvt_f32_ubyte3_e32 v241, v185
	v_pk_mul_f32 v[234:235], v[234:235], v[238:239]
	v_pk_mul_f32 v[236:237], v[236:237], v[240:241]
	v_pk_mul_f32 v[84:85], v[84:85], v[234:235]
	v_pk_mul_f32 v[86:87], v[86:87], v[236:237]
	s_waitcnt vmcnt(10)
	v_cvt_f32_ubyte0_e32 v234, v194
	v_cvt_f32_ubyte1_e32 v235, v194
	v_cvt_f32_ubyte2_e32 v236, v194
	v_cvt_f32_ubyte3_e32 v237, v194
	v_rcp_iflag_f32_e32 v234, v234
	v_rcp_iflag_f32_e32 v235, v235
	v_rcp_iflag_f32_e32 v236, v236
	v_rcp_iflag_f32_e32 v237, v237
	v_cvt_f32_ubyte0_e32 v238, v192
	v_cvt_f32_ubyte1_e32 v239, v192
	v_cvt_f32_ubyte2_e32 v240, v192
	v_cvt_f32_ubyte3_e32 v241, v192
	v_pk_mul_f32 v[234:235], v[234:235], v[238:239]
	v_pk_mul_f32 v[236:237], v[236:237], v[240:241]
	v_pk_mul_f32 v[80:81], v[80:81], v[234:235]
	v_pk_mul_f32 v[82:83], v[82:83], v[236:237]
	v_cvt_f32_ubyte0_e32 v234, v195
	v_cvt_f32_ubyte1_e32 v235, v195
	v_cvt_f32_ubyte2_e32 v236, v195
	v_cvt_f32_ubyte3_e32 v237, v195
	v_rcp_iflag_f32_e32 v234, v234
	v_rcp_iflag_f32_e32 v235, v235
	v_rcp_iflag_f32_e32 v236, v236
	v_rcp_iflag_f32_e32 v237, v237
	v_cvt_f32_ubyte0_e32 v238, v193
	v_cvt_f32_ubyte1_e32 v239, v193
	v_cvt_f32_ubyte2_e32 v240, v193
	v_cvt_f32_ubyte3_e32 v241, v193
	v_pk_mul_f32 v[234:235], v[234:235], v[238:239]
	v_pk_mul_f32 v[236:237], v[236:237], v[240:241]
	v_pk_mul_f32 v[76:77], v[76:77], v[234:235]
	v_pk_mul_f32 v[78:79], v[78:79], v[236:237]
	s_waitcnt vmcnt(8)
	v_cvt_f32_ubyte0_e32 v234, v198
	v_cvt_f32_ubyte1_e32 v235, v198
	v_cvt_f32_ubyte2_e32 v236, v198
	v_cvt_f32_ubyte3_e32 v237, v198
	v_rcp_iflag_f32_e32 v234, v234
	v_rcp_iflag_f32_e32 v235, v235
	v_rcp_iflag_f32_e32 v236, v236
	v_rcp_iflag_f32_e32 v237, v237
	v_cvt_f32_ubyte0_e32 v238, v196
	v_cvt_f32_ubyte1_e32 v239, v196
	v_cvt_f32_ubyte2_e32 v240, v196
	v_cvt_f32_ubyte3_e32 v241, v196
	v_pk_mul_f32 v[234:235], v[234:235], v[238:239]
	v_pk_mul_f32 v[236:237], v[236:237], v[240:241]
	v_pk_mul_f32 v[72:73], v[72:73], v[234:235]
	v_pk_mul_f32 v[74:75], v[74:75], v[236:237]
	v_cvt_f32_ubyte0_e32 v234, v199
	v_cvt_f32_ubyte1_e32 v235, v199
	v_cvt_f32_ubyte2_e32 v236, v199
	v_cvt_f32_ubyte3_e32 v237, v199
	v_rcp_iflag_f32_e32 v234, v234
	v_rcp_iflag_f32_e32 v235, v235
	v_rcp_iflag_f32_e32 v236, v236
	v_rcp_iflag_f32_e32 v237, v237
	v_cvt_f32_ubyte0_e32 v238, v197
	v_cvt_f32_ubyte1_e32 v239, v197
	v_cvt_f32_ubyte2_e32 v240, v197
	v_cvt_f32_ubyte3_e32 v241, v197
	v_pk_mul_f32 v[234:235], v[234:235], v[238:239]
	v_pk_mul_f32 v[236:237], v[236:237], v[240:241]
	v_pk_mul_f32 v[68:69], v[68:69], v[234:235]
	v_pk_mul_f32 v[70:71], v[70:71], v[236:237]
	s_waitcnt vmcnt(6)
	v_cvt_f32_ubyte0_e32 v234, v202
	v_cvt_f32_ubyte1_e32 v235, v202
	v_cvt_f32_ubyte2_e32 v236, v202
	v_cvt_f32_ubyte3_e32 v237, v202
	v_rcp_iflag_f32_e32 v234, v234
	v_rcp_iflag_f32_e32 v235, v235
	v_rcp_iflag_f32_e32 v236, v236
	v_rcp_iflag_f32_e32 v237, v237
	v_cvt_f32_ubyte0_e32 v238, v200
	v_cvt_f32_ubyte1_e32 v239, v200
	v_cvt_f32_ubyte2_e32 v240, v200
	v_cvt_f32_ubyte3_e32 v241, v200
	v_pk_mul_f32 v[234:235], v[234:235], v[238:239]
	v_pk_mul_f32 v[236:237], v[236:237], v[240:241]
	v_pk_mul_f32 v[64:65], v[64:65], v[234:235]
	v_pk_mul_f32 v[66:67], v[66:67], v[236:237]
	v_cvt_f32_ubyte0_e32 v234, v203
	v_cvt_f32_ubyte1_e32 v235, v203
	v_cvt_f32_ubyte2_e32 v236, v203
	v_cvt_f32_ubyte3_e32 v237, v203
	v_rcp_iflag_f32_e32 v234, v234
	v_rcp_iflag_f32_e32 v235, v235
	v_rcp_iflag_f32_e32 v236, v236
	v_rcp_iflag_f32_e32 v237, v237
	v_cvt_f32_ubyte0_e32 v238, v201
	v_cvt_f32_ubyte1_e32 v239, v201
	v_cvt_f32_ubyte2_e32 v240, v201
	v_cvt_f32_ubyte3_e32 v241, v201
	v_pk_mul_f32 v[234:235], v[234:235], v[238:239]
	v_pk_mul_f32 v[236:237], v[236:237], v[240:241]
	v_pk_mul_f32 v[60:61], v[60:61], v[234:235]
	v_pk_mul_f32 v[62:63], v[62:63], v[236:237]
	s_waitcnt vmcnt(4)
	v_cvt_f32_ubyte0_e32 v234, v206
	v_cvt_f32_ubyte1_e32 v235, v206
	v_cvt_f32_ubyte2_e32 v236, v206
	v_cvt_f32_ubyte3_e32 v237, v206
	v_rcp_iflag_f32_e32 v234, v234
	v_rcp_iflag_f32_e32 v235, v235
	v_rcp_iflag_f32_e32 v236, v236
	v_rcp_iflag_f32_e32 v237, v237
	v_cvt_f32_ubyte0_e32 v238, v204
	v_cvt_f32_ubyte1_e32 v239, v204
	v_cvt_f32_ubyte2_e32 v240, v204
	v_cvt_f32_ubyte3_e32 v241, v204
	v_pk_mul_f32 v[234:235], v[234:235], v[238:239]
	v_pk_mul_f32 v[236:237], v[236:237], v[240:241]
	v_pk_mul_f32 v[56:57], v[56:57], v[234:235]
	v_pk_mul_f32 v[58:59], v[58:59], v[236:237]
	v_cvt_f32_ubyte0_e32 v234, v207
	v_cvt_f32_ubyte1_e32 v235, v207
	v_cvt_f32_ubyte2_e32 v236, v207
	v_cvt_f32_ubyte3_e32 v237, v207
	v_rcp_iflag_f32_e32 v234, v234
	v_rcp_iflag_f32_e32 v235, v235
	v_rcp_iflag_f32_e32 v236, v236
	v_rcp_iflag_f32_e32 v237, v237
	v_cvt_f32_ubyte0_e32 v238, v205
	v_cvt_f32_ubyte1_e32 v239, v205
	v_cvt_f32_ubyte2_e32 v240, v205
	v_cvt_f32_ubyte3_e32 v241, v205
	v_pk_mul_f32 v[234:235], v[234:235], v[238:239]
	v_pk_mul_f32 v[236:237], v[236:237], v[240:241]
	v_pk_mul_f32 v[52:53], v[52:53], v[234:235]
	v_pk_mul_f32 v[54:55], v[54:55], v[236:237]
	s_waitcnt vmcnt(2)
	v_cvt_f32_ubyte0_e32 v234, v228
	v_cvt_f32_ubyte1_e32 v235, v228
	v_cvt_f32_ubyte2_e32 v236, v228
	v_cvt_f32_ubyte3_e32 v237, v228
	v_rcp_iflag_f32_e32 v234, v234
	v_rcp_iflag_f32_e32 v235, v235
	v_rcp_iflag_f32_e32 v236, v236
	v_rcp_iflag_f32_e32 v237, v237
	v_cvt_f32_ubyte0_e32 v238, v226
	v_cvt_f32_ubyte1_e32 v239, v226
	v_cvt_f32_ubyte2_e32 v240, v226
	v_cvt_f32_ubyte3_e32 v241, v226
	v_pk_mul_f32 v[234:235], v[234:235], v[238:239]
	v_pk_mul_f32 v[236:237], v[236:237], v[240:241]
	v_pk_mul_f32 v[48:49], v[48:49], v[234:235]
	v_pk_mul_f32 v[50:51], v[50:51], v[236:237]
	v_cvt_f32_ubyte0_e32 v234, v229
	v_cvt_f32_ubyte1_e32 v235, v229
	v_cvt_f32_ubyte2_e32 v236, v229
	v_cvt_f32_ubyte3_e32 v237, v229
	v_rcp_iflag_f32_e32 v234, v234
	v_rcp_iflag_f32_e32 v235, v235
	v_rcp_iflag_f32_e32 v236, v236
	v_rcp_iflag_f32_e32 v237, v237
	v_cvt_f32_ubyte0_e32 v238, v227
	v_cvt_f32_ubyte1_e32 v239, v227
	v_cvt_f32_ubyte2_e32 v240, v227
	v_cvt_f32_ubyte3_e32 v241, v227
	v_pk_mul_f32 v[234:235], v[234:235], v[238:239]
	v_pk_mul_f32 v[236:237], v[236:237], v[240:241]
	v_pk_mul_f32 v[44:45], v[44:45], v[234:235]
	v_pk_mul_f32 v[46:47], v[46:47], v[236:237]
	s_waitcnt vmcnt(0)
	v_cvt_f32_ubyte0_e32 v234, v232
	v_cvt_f32_ubyte1_e32 v235, v232
	v_cvt_f32_ubyte2_e32 v236, v232
	v_cvt_f32_ubyte3_e32 v237, v232
	v_rcp_iflag_f32_e32 v234, v234
	v_rcp_iflag_f32_e32 v235, v235
	v_rcp_iflag_f32_e32 v236, v236
	v_rcp_iflag_f32_e32 v237, v237
	v_cvt_f32_ubyte0_e32 v238, v230
	v_cvt_f32_ubyte1_e32 v239, v230
	v_cvt_f32_ubyte2_e32 v240, v230
	v_cvt_f32_ubyte3_e32 v241, v230
	v_pk_mul_f32 v[234:235], v[234:235], v[238:239]
	v_pk_mul_f32 v[236:237], v[236:237], v[240:241]
	v_pk_mul_f32 v[40:41], v[40:41], v[234:235]
	v_pk_mul_f32 v[42:43], v[42:43], v[236:237]
	v_cvt_f32_ubyte0_e32 v234, v233
	v_cvt_f32_ubyte1_e32 v235, v233
	v_cvt_f32_ubyte2_e32 v236, v233
	v_cvt_f32_ubyte3_e32 v237, v233
	v_rcp_iflag_f32_e32 v234, v234
	v_rcp_iflag_f32_e32 v235, v235
	v_rcp_iflag_f32_e32 v236, v236
	v_rcp_iflag_f32_e32 v237, v237
	v_cvt_f32_ubyte0_e32 v238, v231
	v_cvt_f32_ubyte1_e32 v239, v231
	v_cvt_f32_ubyte2_e32 v240, v231
	v_cvt_f32_ubyte3_e32 v241, v231
	v_pk_mul_f32 v[234:235], v[234:235], v[238:239]
	v_pk_mul_f32 v[236:237], v[236:237], v[240:241]
	v_pk_mul_f32 v[36:37], v[36:37], v[234:235]
	v_pk_mul_f32 v[38:39], v[38:39], v[236:237]
	s_nop 3
	s_andn2_b64 vcc, exec, s[36:37]
	s_mov_b64 s[36:37], s[24:25]
	s_cbranch_vccnz .LBB0_623
